# tile scheduler: the float reciprocal of the (always 8) group size replaced by its constant
# baseline (speedup 1.0000x reference)
.LBB0_268:
	s_add_i32 s75, s75, 1
	v_readlane_b32 s40, v252, 34
	s_mul_i32 s40, s75, s40
	s_mul_hi_u32 s41, s75, s3
	s_add_i32 s41, s41, s40
	s_mul_i32 s40, s75, s3
	v_readlane_b32 s42, v251, 0
	s_add_u32 s40, s40, s42
	v_readlane_b32 s42, v252, 33
	s_addc_u32 s41, s41, s42
	v_mov_b64_e32 v[2:3], 0x1600
	v_cmp_lt_i64_e64 s[42:43], s[40:41], v[2:3]
	v_mov_b64_e32 v[2:3], 0x15ff
	v_cmp_gt_i64_e32 vcc, s[40:41], v[2:3]
	s_cbranch_vccnz .LBB0_270
	s_ashr_i32 s41, s40, 31
	s_lshr_b32 s41, s41, 29
	s_add_i32 s41, s40, s41
	s_waitcnt lgkmcnt(0)
	s_ashr_i32 s50, s41, 3
	s_and_b32 s41, s41, -8
	s_sub_i32 s40, s40, s41
	s_cmp_lt_i32 s40, 0
	s_movk_i32 s41, 0x2c1
	s_cselect_b32 s41, s41, 0x2c0
	s_mul_i32 s40, s40, s41
	s_add_i32 s40, s40, s50
	s_mul_hi_i32 s41, s40, 0x2e8ba2e9
	s_lshr_b32 s50, s41, 31
	s_ashr_i32 s41, s41, 6
	s_add_i32 s41, s41, s50
	s_lshl_b32 s50, s41, 3
	s_sub_i32 s51, 0x80, s50
	s_min_i32 s51, s51, 8
	s_abs_i32 s52, s51
	s_sub_i32 s54, 0, s52
	s_mulk_i32 s41, 0x160
	s_sub_i32 s40, s40, s41
	s_abs_i32 s41, s40
	s_xor_b32 s53, s40, s51
	s_ashr_i32 s53, s53, 31
	s_mov_b32 s55, 0x1fffffc0
	s_mul_i32 s54, s54, s55
	s_mul_hi_u32 s54, s55, s54
	s_add_i32 s55, s55, s54
	s_mul_hi_u32 s54, s41, s55
	s_mul_i32 s55, s54, s52
	s_sub_i32 s41, s41, s55
	s_add_i32 s60, s54, 1
	s_sub_i32 s55, s41, s52
	s_cmp_ge_u32 s41, s52
	s_cselect_b32 s54, s60, s54
	s_cselect_b32 s41, s55, s41
	s_add_i32 s55, s54, 1
	s_cmp_ge_u32 s41, s52
	s_cselect_b32 s41, s55, s54
	s_xor_b32 s41, s41, s53
	s_sub_i32 s77, s41, s53
	s_mul_i32 s41, s77, s51
	s_sub_i32 s40, s40, s41
	s_add_i32 s78, s50, s40

.LBB0_299:
	s_ashr_i32 s38, s42, 3
	s_add_i32 s38, s45, s38
	s_ashr_i32 s39, s38, 31
	s_lshr_b32 s39, s39, 25
	s_add_i32 s39, s38, s39
	s_ashr_i32 s42, s39, 7
	s_lshl_b32 s42, s42, 3
	s_sub_i32 s43, 16, s42
	s_min_i32 s43, s43, 8
	s_abs_i32 s45, s43
	s_waitcnt lgkmcnt(0)
	s_sub_i32 s51, 0, s45
	s_and_b32 s39, s39, 0xffffff80
	s_sub_i32 s38, s38, s39
	s_abs_i32 s39, s38
	s_xor_b32 s50, s38, s43
	s_ashr_i32 s50, s50, 31
	s_mov_b32 s52, 0x1fffffc0
	s_mul_i32 s51, s51, s52
	s_mul_hi_u32 s51, s52, s51
	s_add_i32 s52, s52, s51
	s_mul_hi_u32 s51, s39, s52
	s_mul_i32 s52, s51, s45
	s_sub_i32 s39, s39, s52
	s_add_i32 s53, s51, 1
	s_sub_i32 s52, s39, s45
	s_cmp_ge_u32 s39, s45
	s_cselect_b32 s51, s53, s51
	s_cselect_b32 s39, s52, s39
	s_add_i32 s52, s51, 1
	s_cmp_ge_u32 s39, s45
	s_cselect_b32 s39, s52, s51
	s_xor_b32 s39, s39, s50
	s_sub_i32 s64, s39, s50
	s_mul_i32 s39, s64, s43
	s_sub_i32 s38, s38, s39
	s_add_i32 s65, s42, s38

.LBB0_374:
	s_ashr_i32 s30, s34, 3
	s_add_i32 s30, s44, s30
	s_ashr_i32 s31, s30, 31
	s_lshr_b32 s31, s31, 26
	s_add_i32 s31, s30, s31
	s_ashr_i32 s34, s31, 6
	s_lshl_b32 s34, s34, 3
	s_sub_i32 s35, 0x80, s34
	s_min_i32 s35, s35, 8
	s_abs_i32 s44, s35
	s_sub_i32 s52, 0, s44
	s_andn2_b32 s31, s31, 63
	s_sub_i32 s30, s30, s31
	s_abs_i32 s31, s30
	s_xor_b32 s45, s30, s35
	s_ashr_i32 s45, s45, 31
	s_mov_b32 s53, 0x1fffffc0
	s_mul_i32 s52, s52, s53
	s_mul_hi_u32 s52, s53, s52
	s_add_i32 s53, s53, s52
	s_mul_hi_u32 s52, s31, s53
	s_mul_i32 s53, s52, s44
	s_sub_i32 s31, s31, s53
	s_add_i32 s63, s52, 1
	s_sub_i32 s53, s31, s44
	s_cmp_ge_u32 s31, s44
	s_cselect_b32 s52, s63, s52
	s_cselect_b32 s31, s53, s31
	s_add_i32 s53, s52, 1
	s_cmp_ge_u32 s31, s44
	s_cselect_b32 s31, s53, s52
	s_xor_b32 s31, s31, s45
	s_sub_i32 s63, s31, s45
	s_mul_i32 s31, s63, s35
	s_sub_i32 s30, s30, s31
	s_add_i32 s64, s34, s30

.LBB0_446:
	s_add_i32 s85, s85, 1
	v_readlane_b32 s1, v252, 34
	s_mul_i32 s1, s85, s1
	s_mul_hi_u32 s2, s85, s3
	s_add_i32 s2, s2, s1
	s_mul_i32 s1, s85, s3
	v_readlane_b32 s11, v251, 0
	s_add_u32 s26, s1, s11
	v_readlane_b32 s1, v252, 33
	s_addc_u32 s27, s2, s1
	s_waitcnt lgkmcnt(0)
	v_mov_b64_e32 v[130:131], 0xa80
	v_cmp_lt_i64_e64 s[46:47], s[26:27], v[130:131]
	v_mov_b64_e32 v[130:131], 0xa7f
	v_cmp_gt_i64_e64 s[44:45], s[26:27], v[130:131]
	s_and_b64 vcc, exec, s[44:45]
	s_cbranch_vccnz .LBB0_448
	s_ashr_i32 s1, s26, 31
	s_lshr_b32 s1, s1, 29
	s_add_i32 s1, s26, s1
	s_ashr_i32 s2, s1, 3
	s_and_b32 s1, s1, -8
	s_sub_i32 s1, s26, s1
	s_cmp_lt_i32 s1, 0
	s_movk_i32 s11, 0x151
	s_cselect_b32 s11, s11, 0x150
	s_mul_i32 s1, s1, s11
	s_add_i32 s1, s1, s2
	s_mul_hi_i32 s2, s1, 0x30c30c31
	s_lshr_b32 s11, s2, 31
	s_ashr_i32 s2, s2, 5
	s_add_i32 s2, s2, s11
	s_lshl_b32 s11, s2, 3
	s_sub_i32 s14, 0x80, s11
	s_min_i32 s14, s14, 8
	s_abs_i32 s15, s14
	s_sub_i32 s20, 0, s15
	s_mulk_i32 s2, 0xa8
	s_sub_i32 s1, s1, s2
	s_abs_i32 s2, s1
	s_xor_b32 s18, s1, s14
	s_ashr_i32 s18, s18, 31
	s_mov_b32 s21, 0x1fffffc0
	s_mul_i32 s20, s20, s21
	s_mul_hi_u32 s20, s21, s20
	s_add_i32 s21, s21, s20
	s_mul_hi_u32 s20, s2, s21
	s_mul_i32 s21, s20, s15
	s_sub_i32 s2, s2, s21
	s_add_i32 s25, s20, 1
	s_sub_i32 s21, s2, s15
	s_cmp_ge_u32 s2, s15
	s_cselect_b32 s20, s25, s20
	s_cselect_b32 s2, s21, s2
	s_add_i32 s21, s20, 1
	s_cmp_ge_u32 s2, s15
	s_cselect_b32 s2, s21, s20
	s_xor_b32 s2, s2, s18
	s_sub_i32 s86, s2, s18
	s_mul_i32 s2, s86, s14
	s_sub_i32 s1, s1, s2
	s_add_i32 s87, s11, s1

.LBB0_491:
	s_ashr_i32 s40, s46, 3
	s_add_i32 s40, s52, s40
	s_ashr_i32 s41, s40, 31
	s_lshr_b32 s41, s41, 26
	s_add_i32 s41, s40, s41
	s_ashr_i32 s46, s41, 6
	s_lshl_b32 s46, s46, 3
	s_sub_i32 s47, 64, s46
	s_min_i32 s47, s47, 8
	s_abs_i32 s52, s47
	s_sub_i32 s54, 0, s52
	s_andn2_b32 s41, s41, 63
	s_sub_i32 s40, s40, s41
	s_abs_i32 s41, s40
	s_xor_b32 s53, s40, s47
	s_ashr_i32 s53, s53, 31
	s_mov_b32 s55, 0x1fffffc0
	s_mul_i32 s54, s54, s55
	s_mul_hi_u32 s54, s55, s54
	s_add_i32 s55, s55, s54
	s_mul_hi_u32 s54, s41, s55
	s_mul_i32 s55, s54, s52
	s_sub_i32 s41, s41, s55
	s_add_i32 s77, s54, 1
	s_sub_i32 s55, s41, s52
	s_cmp_ge_u32 s41, s52
	s_cselect_b32 s54, s77, s54
	s_cselect_b32 s41, s55, s41
	s_add_i32 s55, s54, 1
	s_cmp_ge_u32 s41, s52
	s_cselect_b32 s41, s55, s54
	s_xor_b32 s41, s41, s53
	s_sub_i32 s77, s41, s53
	s_mul_i32 s41, s77, s47
	s_sub_i32 s40, s40, s41
	s_add_i32 s78, s46, s40

.LBB0_524:
	s_ashr_i32 s40, s44, 3
	s_add_i32 s40, s47, s40
	s_ashr_i32 s41, s40, 31
	s_lshr_b32 s41, s41, 25
	s_add_i32 s41, s40, s41
	s_ashr_i32 s44, s41, 7
	s_lshl_b32 s44, s44, 3
	s_sub_i32 s45, 32, s44
	s_min_i32 s45, s45, 8
	s_abs_i32 s47, s45
	s_sub_i32 s53, 0, s47
	s_and_b32 s41, s41, 0xffffff80
	s_sub_i32 s40, s40, s41
	s_abs_i32 s41, s40
	s_xor_b32 s52, s40, s45
	s_ashr_i32 s52, s52, 31
	s_mov_b32 s54, 0x1fffffc0
	s_mul_i32 s53, s53, s54
	s_mul_hi_u32 s53, s54, s53
	s_add_i32 s54, s54, s53
	s_mul_hi_u32 s53, s41, s54
	s_mul_i32 s54, s53, s47
	s_sub_i32 s41, s41, s54
	s_add_i32 s55, s53, 1
	s_sub_i32 s54, s41, s47
	s_cmp_ge_u32 s41, s47
	s_cselect_b32 s53, s55, s53
	s_cselect_b32 s41, s54, s41
	s_add_i32 s54, s53, 1
	s_cmp_ge_u32 s41, s47
	s_cselect_b32 s41, s54, s53
	s_xor_b32 s41, s41, s52
	s_sub_i32 s77, s41, s52
	s_mul_i32 s41, s77, s45
	s_sub_i32 s40, s40, s41
	s_add_i32 s78, s44, s40

.LBB0_700:
	s_ashr_i32 s40, s44, 3
	s_add_i32 s40, s52, s40
	s_ashr_i32 s41, s40, 31
	s_lshr_b32 s41, s41, 29
	s_add_i32 s41, s40, s41
	s_and_b32 s41, s41, -8
	s_sub_i32 s44, 0x200, s41
	s_min_i32 s44, s44, 8
	s_abs_i32 s45, s44
	s_sub_i32 s53, 0, s45
	s_sub_i32 s41, s40, s41
	s_abs_i32 s52, s41
	s_xor_b32 s41, s41, s44
	s_ashr_i32 s41, s41, 31
	s_mov_b32 s54, 0x1fffffc0
	s_mul_i32 s53, s53, s54
	s_mul_hi_u32 s53, s54, s53
	s_add_i32 s54, s54, s53
	s_mul_hi_u32 s53, s52, s54
	s_mul_i32 s54, s53, s45
	s_sub_i32 s52, s52, s54
	s_add_i32 s55, s53, 1
	s_sub_i32 s54, s52, s45
	s_cmp_ge_u32 s52, s45
	s_cselect_b32 s53, s55, s53
	s_cselect_b32 s52, s54, s52
	s_add_i32 s54, s53, 1
	s_cmp_ge_u32 s52, s45
	s_cselect_b32 s45, s54, s53
	s_xor_b32 s45, s45, s41
	s_sub_i32 s69, s45, s41
	s_mul_i32 s41, s69, s44
	s_sub_i32 s70, s40, s41

.LBB0_885:
	s_ashr_i32 s30, s34, 3
	s_add_i32 s30, s40, s30
	s_ashr_i32 s31, s30, 31
	s_lshr_b32 s31, s31, 26
	s_add_i32 s31, s30, s31
	s_ashr_i32 s34, s31, 6
	s_lshl_b32 s34, s34, 3
	s_sub_i32 s35, 0x80, s34
	s_min_i32 s35, s35, 8
	s_abs_i32 s40, s35
	s_sub_i32 s46, 0, s40
	s_andn2_b32 s31, s31, 63
	s_sub_i32 s30, s30, s31
	s_abs_i32 s31, s30
	s_xor_b32 s41, s30, s35
	s_ashr_i32 s41, s41, 31
	s_mov_b32 s47, 0x1fffffc0
	s_mul_i32 s46, s46, s47
	s_mul_hi_u32 s46, s47, s46
	s_add_i32 s47, s47, s46
	s_mul_hi_u32 s46, s31, s47
	s_mul_i32 s47, s46, s40
	s_sub_i32 s31, s31, s47
	s_add_i32 s63, s46, 1
	s_sub_i32 s47, s31, s40
	s_cmp_ge_u32 s31, s40
	s_cselect_b32 s46, s63, s46
	s_cselect_b32 s31, s47, s31
	s_add_i32 s47, s46, 1
	s_cmp_ge_u32 s31, s40
	s_cselect_b32 s31, s47, s46
	s_xor_b32 s31, s31, s41
	s_sub_i32 s63, s31, s41
	s_mul_i32 s31, s63, s35
	s_sub_i32 s30, s30, s31
	s_add_i32 s64, s34, s30

.LBB0_960:
	s_ashr_i32 s30, s34, 3
	s_add_i32 s30, s40, s30
	s_ashr_i32 s31, s30, 31
	s_lshr_b32 s31, s31, 27
	s_add_i32 s31, s30, s31
	s_ashr_i32 s34, s31, 5
	s_lshl_b32 s34, s34, 3
	s_sub_i32 s35, 0x80, s34
	s_min_i32 s35, s35, 8
	s_abs_i32 s40, s35
	s_sub_i32 s54, 0, s40
	s_andn2_b32 s31, s31, 31
	s_sub_i32 s30, s30, s31
	s_abs_i32 s31, s30
	s_xor_b32 s41, s30, s35
	s_ashr_i32 s41, s41, 31
	s_mov_b32 s55, 0x1fffffc0
	s_mul_i32 s54, s54, s55
	s_mul_hi_u32 s54, s55, s54
	s_add_i32 s55, s55, s54
	s_mul_hi_u32 s54, s31, s55
	s_mul_i32 s55, s54, s40
	s_sub_i32 s31, s31, s55
	s_add_i32 s56, s54, 1
	s_sub_i32 s55, s31, s40
	s_cmp_ge_u32 s31, s40
	s_cselect_b32 s54, s56, s54
	s_cselect_b32 s31, s55, s31
	s_add_i32 s55, s54, 1
	s_cmp_ge_u32 s31, s40
	s_cselect_b32 s31, s55, s54
	s_xor_b32 s31, s31, s41
	s_sub_i32 s70, s31, s41
	s_mul_i32 s31, s70, s35
	s_sub_i32 s30, s30, s31
	s_add_i32 s71, s34, s30

.LBB0_1067:
	s_ashr_i32 s21, s21, 3
	s_add_i32 s21, s35, s21
	s_ashr_i32 s30, s21, 31
	s_lshr_b32 s30, s30, 26
	s_add_i32 s30, s21, s30
	s_ashr_i32 s31, s30, 6
	s_lshl_b32 s31, s31, 3
	s_sub_i32 s34, 0x80, s31
	s_min_i32 s34, s34, 8
	s_abs_i32 s35, s34
	s_sub_i32 s45, 0, s35
	s_andn2_b32 s30, s30, 63
	s_sub_i32 s21, s21, s30
	s_abs_i32 s30, s21
	s_xor_b32 s44, s21, s34
	s_ashr_i32 s44, s44, 31
	s_mov_b32 s54, 0x1fffffc0
	s_mul_i32 s45, s45, s54
	s_mul_hi_u32 s45, s54, s45
	s_add_i32 s54, s54, s45
	s_mul_hi_u32 s45, s30, s54
	s_mul_i32 s54, s45, s35
	s_sub_i32 s30, s30, s54
	s_add_i32 s55, s45, 1
	s_sub_i32 s54, s30, s35
	s_cmp_ge_u32 s30, s35
	s_cselect_b32 s45, s55, s45
	s_cselect_b32 s30, s54, s30
	s_add_i32 s54, s45, 1
	s_cmp_ge_u32 s30, s35
	s_cselect_b32 s30, s54, s45
	s_xor_b32 s30, s30, s44
	s_sub_i32 s67, s30, s44
	s_mul_i32 s30, s67, s34
	s_sub_i32 s21, s21, s30
	s_add_i32 s68, s31, s21

.LBB0_1139:
	s_add_i32 s73, s73, 1
	v_readlane_b32 s40, v252, 34
	s_mul_i32 s40, s73, s40
	s_mul_hi_u32 s41, s73, s3
	s_add_i32 s41, s41, s40
	s_mul_i32 s40, s73, s3
	v_readlane_b32 s42, v251, 0
	s_add_u32 s40, s40, s42
	v_readlane_b32 s42, v252, 33
	s_addc_u32 s41, s41, s42
	v_mov_b64_e32 v[2:3], 0x1600
	v_cmp_lt_i64_e64 s[42:43], s[40:41], v[2:3]
	v_mov_b64_e32 v[2:3], 0x15ff
	v_cmp_gt_i64_e32 vcc, s[40:41], v[2:3]
	s_cbranch_vccnz .LBB0_1141
	s_ashr_i32 s41, s40, 31
	s_lshr_b32 s41, s41, 29
	s_add_i32 s41, s40, s41
	s_ashr_i32 s48, s41, 3
	s_and_b32 s41, s41, -8
	s_sub_i32 s40, s40, s41
	s_cmp_lt_i32 s40, 0
	s_movk_i32 s41, 0x2c1
	s_cselect_b32 s41, s41, 0x2c0
	s_mul_i32 s40, s40, s41
	s_add_i32 s40, s40, s48
	s_mul_hi_i32 s41, s40, 0x2e8ba2e9
	s_lshr_b32 s48, s41, 31
	s_ashr_i32 s41, s41, 6
	s_add_i32 s41, s41, s48
	s_lshl_b32 s48, s41, 3
	s_sub_i32 s49, 0x80, s48
	s_min_i32 s49, s49, 8
	s_abs_i32 s50, s49
	s_sub_i32 s52, 0, s50
	s_mulk_i32 s41, 0x160
	s_sub_i32 s40, s40, s41
	s_abs_i32 s41, s40
	s_xor_b32 s51, s40, s49
	s_ashr_i32 s51, s51, 31
	s_mov_b32 s53, 0x1fffffc0
	s_mul_i32 s52, s52, s53
	s_mul_hi_u32 s52, s53, s52
	s_add_i32 s53, s53, s52
	s_mul_hi_u32 s52, s41, s53
	s_mul_i32 s53, s52, s50
	s_sub_i32 s41, s41, s53
	s_add_i32 s58, s52, 1
	s_sub_i32 s53, s41, s50
	s_cmp_ge_u32 s41, s50
	s_cselect_b32 s52, s58, s52
	s_cselect_b32 s41, s53, s41
	s_add_i32 s53, s52, 1
	s_cmp_ge_u32 s41, s50
	s_cselect_b32 s41, s53, s52
	s_xor_b32 s41, s41, s51
	s_sub_i32 s75, s41, s51
	s_mul_i32 s41, s75, s49
	s_sub_i32 s40, s40, s41
	s_add_i32 s76, s48, s40

.LBB0_1220:
	s_ashr_i32 s30, s34, 3
	s_add_i32 s30, s40, s30
	s_ashr_i32 s31, s30, 31
	s_lshr_b32 s31, s31, 26
	s_add_i32 s31, s30, s31
	s_ashr_i32 s34, s31, 6
	s_lshl_b32 s34, s34, 3
	s_sub_i32 s35, 0x80, s34
	s_min_i32 s35, s35, 8
	s_abs_i32 s40, s35
	s_sub_i32 s52, 0, s40
	s_andn2_b32 s31, s31, 63
	s_sub_i32 s30, s30, s31
	s_abs_i32 s31, s30
	s_xor_b32 s41, s30, s35
	s_ashr_i32 s41, s41, 31
	s_mov_b32 s53, 0x1fffffc0
	s_mul_i32 s52, s52, s53
	s_mul_hi_u32 s52, s53, s52
	s_add_i32 s53, s53, s52
	s_mul_hi_u32 s52, s31, s53
	s_mul_i32 s53, s52, s40
	s_sub_i32 s31, s31, s53
	s_add_i32 s63, s52, 1
	s_sub_i32 s53, s31, s40
	s_cmp_ge_u32 s31, s40
	s_cselect_b32 s52, s63, s52
	s_cselect_b32 s31, s53, s31
	s_add_i32 s53, s52, 1
	s_cmp_ge_u32 s31, s40
	s_cselect_b32 s31, s53, s52
	s_xor_b32 s31, s31, s41
	s_sub_i32 s63, s31, s41
	s_mul_i32 s31, s63, s35
	s_sub_i32 s30, s30, s31
	s_add_i32 s64, s34, s30
